# v22 plus gamma/beta waited once before the loop; in-loop store wait no longer drains the previous iteration's stores
# baseline (speedup 1.0000x reference)
.LBB1_4:
	s_or_b64 exec, exec, s[4:5]
	s_mov_b32 s3, 0x927c
	v_cmp_gt_i32_e32 vcc, s3, v62
	s_waitcnt lgkmcnt(0)
	s_barrier
	s_and_saveexec_b64 s[4:5], vcc
	s_cbranch_execz .LBB1_7
	s_load_dwordx4 s[4:7], s[0:1], 0x30
	v_and_b32_e32 v67, 0x1f0, v58
	v_and_b32_e32 v76, 64, v63
	v_or_b32_e32 v77, v76, v106
	v_lshlrev_b32_e32 v114, 2, v77
	s_waitcnt lgkmcnt(0)
	global_load_dwordx4 v[54:57], v67, s[4:5]
	global_load_dwordx4 v[58:61], v67, s[6:7]
	v_xor_b32_e32 v77, 16, v63
	v_add_u32_e32 v76, 64, v76
	s_load_dwordx2 s[4:5], s[0:1], 0x40
	v_cmp_lt_i32_e32 vcc, v77, v76
	v_lshl_add_u64 v[102:103], s[8:9], 0, v[68:69]
	v_lshl_add_u64 v[104:105], s[10:11], 0, v[68:69]
	s_movk_i32 s1, 0x2800
	v_mov_b32_e32 v67, 0x12200
	v_and_b32_e32 v69, 48, v0
	v_lshrrev_b32_e32 v0, 1, v0
	v_cndmask_b32_e32 v77, v63, v77, vcc
	s_movk_i32 s0, 0x60
	v_mad_u32_u24 v67, v1, s1, v67
	s_movk_i32 s1, 0x120
	v_lshrrev_b32_e32 v73, 5, v70
	v_lshrrev_b32_e32 v70, 2, v70
	v_and_b32_e32 v0, 24, v0
	v_lshlrev_b32_e32 v116, 2, v77
	v_xor_b32_e32 v77, 32, v63
	v_mad_u32_u24 v112, v106, s1, v69
	s_movk_i32 s3, 0x220
	v_mad_u32_u24 v72, v106, s0, v67
	v_mad_u32_u24 v70, v70, s0, v67
	v_sub_u32_e32 v0, 0, v0
	v_cmp_lt_i32_e32 vcc, v77, v76
	s_lshl_b32 s0, s2, 13
	v_mad_u32_u24 v71, v106, s3, v67
	v_mad_u32_u24 v73, v73, s3, v67
	v_and_b32_e32 v74, 0x1f0, v68
	v_and_b32_e32 v75, 48, v68
	v_mad_u32_u24 v65, v65, s1, v67
	v_mad_u32_u24 v67, v106, s1, v67
	v_cndmask_b32_e32 v63, v63, v77, vcc
	v_lshl_add_u32 v1, v1, 21, s0
	s_movk_i32 s0, 0x1c00
	v_add_u32_e32 v0, v112, v0
	v_or_b32_e32 v109, 32, v107
	v_or_b32_e32 v110, 64, v107
	v_or_b32_e32 v111, 0x60, v107
	s_mov_b32 s7, 0x27000
	s_brev_b32 s6, -2
	s_waitcnt lgkmcnt(0)
	s_and_b32 s5, s5, 0xffff
	v_add_u32_e32 v113, 0x9000, v112
	v_or_b32_e32 v115, 64, v114
	v_lshlrev_b32_e32 v117, 2, v63
	v_or3_b32 v118, v1, v68, s0
	s_mov_b64 s[0:1], 0
	s_movk_i32 s3, 0x1000
	s_mov_b32 s8, 0x927b
	v_add_u32_e32 v119, v65, v66
	v_mov_b32_e32 v1, 0
	v_add_u32_e32 v120, v67, v69
	v_add_u32_e32 v121, v73, v74
	v_add_u32_e32 v122, v70, v75
	v_add_u32_e32 v123, v71, v69
	v_add_u32_e32 v124, v72, v69
	v_or_b32_e32 v125, 0x12000, v69
	v_or_b32_e32 v126, 0x12040, v69
	v_or_b32_e32 v127, 0x12080, v69
	v_or_b32_e32 v128, 0x120c0, v69
	v_or_b32_e32 v129, 0x12100, v69
	v_or_b32_e32 v130, 0x12140, v69
	v_or_b32_e32 v131, 0x12180, v69
	v_or_b32_e32 v132, 0x121c0, v69
	s_mov_b32 s2, 0xbf317218
	v_mov_b32_e32 v133, 0x3727c5ac
	v_add_u32_e32 v134, 0x100, v0
	s_waitcnt vmcnt(0)
.LBB1_6:
	s_waitcnt vmcnt(14)
	ds_write_b128 v119, v[38:41]
	s_waitcnt vmcnt(13)
	ds_write_b128 v119, v[42:45] offset:2304
	s_waitcnt vmcnt(12)
	ds_write_b128 v119, v[46:49] offset:4608
	s_waitcnt vmcnt(11)
	ds_write_b128 v119, v[50:53] offset:6912
	ds_bpermute_b32 v42, v107, v64
	ds_bpermute_b32 v43, v109, v64
	ds_bpermute_b32 v44, v110, v64
	v_add_u32_e32 v0, 0x1000, v62
	ds_bpermute_b32 v50, v111, v64
	v_min_i32_e32 v0, 0x927b, v0
	v_lshl_or_b32 v40, v0, 4, v106
	s_waitcnt lgkmcnt(3)
	v_lshlrev_b32_e32 v0, 7, v42
	v_ashrrev_i32_e32 v65, 31, v64
	v_lshl_add_u64 v[46:47], v[98:99], 0, v[0:1]
	s_waitcnt lgkmcnt(2)
	v_lshlrev_b32_e32 v0, 7, v43
	v_lshl_add_u64 v[38:39], v[64:65], 2, v[96:97]
	v_ashrrev_i32_e32 v41, 31, v40
	v_lshl_add_u64 v[48:49], v[98:99], 0, v[0:1]
	s_waitcnt lgkmcnt(1)
	v_lshlrev_b32_e32 v0, 7, v44
	s_waitcnt vmcnt(10)
	v_mov_b32_e32 v68, v108
	v_mov_b32_e32 v66, v108
	s_nop 1
	v_permlane16_swap_b32_e32 v68, v66
	global_load_dword v108, v[38:39], off
	v_lshl_add_u64 v[38:39], v[40:41], 2, v[94:95]
	v_lshl_add_u64 v[64:65], v[100:101], 0, v[0:1]
	s_waitcnt lgkmcnt(0)
	v_lshlrev_b32_e32 v0, 7, v50
	global_load_dword v135, v[38:39], off
	s_nop 0
	global_load_dwordx4 v[38:41], v[46:47], off
	global_load_dwordx4 v[42:45], v[48:49], off
	v_lshl_add_u64 v[70:71], v[100:101], 0, v[0:1]
	global_load_dwordx4 v[46:49], v[64:65], off
	global_load_dwordx4 v[50:53], v[70:71], off
	ds_read_b128 v[70:73], v120
	ds_read_b128 v[74:77], v120 offset:64
	ds_read_b128 v[78:81], v120 offset:4608
	ds_read_b128 v[82:85], v120 offset:4672
	v_add_u32_e32 v0, 0x800, v62
	ds_write_b128 v121, v[2:5]
	ds_write_b128 v121, v[6:9] offset:1088
	ds_write_b128 v121, v[10:13] offset:2176
	ds_write_b128 v121, v[14:17] offset:3264
	ds_write_b128 v121, v[18:21] offset:4352
	ds_write_b128 v121, v[22:25] offset:5440
	s_waitcnt vmcnt(15)
	ds_write_b128 v121, v[26:29] offset:6528
	s_waitcnt vmcnt(14)
	ds_write_b128 v121, v[30:33] offset:7616
	ds_write_b128 v122, v[34:37] offset:8704
	v_min_i32_e32 v2, 0x927b, v0
	v_ashrrev_i32_e32 v3, 31, v2
	v_lshlrev_b64 v[4:5], 13, v[2:3]
	v_lshlrev_b64 v[2:3], 10, v[2:3]
	v_lshl_add_u64 v[18:19], v[102:103], 0, v[4:5]
	v_lshl_add_u64 v[62:63], v[104:105], 0, v[2:3]
	v_add_co_u32_e32 v64, vcc, s3, v18
	global_load_dwordx4 v[2:5], v[18:19], off nt
	global_load_dwordx4 v[6:9], v[18:19], off offset:1024 nt
	global_load_dwordx4 v[10:13], v[18:19], off offset:2048 nt
	global_load_dwordx4 v[14:17], v[18:19], off offset:3072 nt
	v_addc_co_u32_e32 v65, vcc, 0, v19, vcc
	global_load_dwordx4 v[34:37], v[62:63], off nt
	global_load_dwordx4 v[18:21], v[64:65], off nt
	global_load_dwordx4 v[22:25], v[64:65], off offset:1024 nt
	global_load_dwordx4 v[26:29], v[64:65], off offset:2048 nt
	global_load_dwordx4 v[30:33], v[64:65], off offset:3072 nt
	s_waitcnt lgkmcnt(13)
	v_add_f32_e32 v67, v68, v66
	v_mul_f32_e32 v184, 0xc3000000, v67
	s_waitcnt lgkmcnt(12)
	v_cvt_f32_ubyte3_e32 v169, v70
	v_cvt_f32_ubyte2_e32 v168, v70
	v_cvt_f32_ubyte1_e32 v171, v70
	v_cvt_f32_ubyte0_e32 v170, v70
	ds_read_b128 v[62:65], v123
	ds_read_b128 v[86:89], v123 offset:64
	ds_read_b128 v[90:93], v112
	ds_read_b128 v[136:139], v112 offset:4608
	ds_read_b128 v[140:143], v112 offset:9216
	ds_read_b128 v[144:147], v112 offset:13824
	ds_read_b128 v[148:151], v112 offset:18432
	ds_read_b128 v[152:155], v112 offset:23040
	ds_read_b128 v[156:159], v112 offset:27648
	ds_read_b128 v[160:163], v112 offset:32256
	s_waitcnt lgkmcnt(14)
	v_cvt_f32_ubyte1_e32 v165, v78
	v_cvt_f32_ubyte0_e32 v164, v78
	v_cvt_f32_ubyte3_e32 v167, v78
	v_cvt_f32_ubyte2_e32 v166, v78
	v_pk_fma_f32 v[170:171], v[170:171], v[68:69], v[184:185] op_sel_hi:[1,0,0]
	v_pk_fma_f32 v[168:169], v[168:169], v[68:69], v[184:185] op_sel_hi:[1,0,0]
	v_pk_fma_f32 v[164:165], v[164:165], v[66:67], v[170:171] op_sel_hi:[1,0,1]
	v_pk_fma_f32 v[166:167], v[166:167], v[66:67], v[168:169] op_sel_hi:[1,0,1]
	v_cvt_f32_ubyte1_e32 v169, v79
	v_cvt_f32_ubyte0_e32 v168, v79
	v_cvt_f32_ubyte3_e32 v171, v79
	v_cvt_f32_ubyte2_e32 v170, v79
	v_cvt_f32_ubyte3_e32 v79, v71
	v_cvt_f32_ubyte2_e32 v78, v71
	v_cvt_f32_ubyte1_e32 v173, v71
	v_cvt_f32_ubyte0_e32 v172, v71
	v_pk_fma_f32 v[70:71], v[172:173], v[68:69], v[184:185] op_sel_hi:[1,0,0]
	v_pk_fma_f32 v[78:79], v[78:79], v[68:69], v[184:185] op_sel_hi:[1,0,0]
	v_cvt_f32_ubyte3_e32 v173, v72
	v_cvt_f32_ubyte2_e32 v172, v72
	v_cvt_f32_ubyte1_e32 v175, v72
	v_cvt_f32_ubyte0_e32 v174, v72
	v_pk_fma_f32 v[170:171], v[170:171], v[66:67], v[78:79] op_sel_hi:[1,0,1]
	v_pk_fma_f32 v[168:169], v[168:169], v[66:67], v[70:71] op_sel_hi:[1,0,1]
	v_cvt_f32_ubyte1_e32 v71, v80
	v_cvt_f32_ubyte0_e32 v70, v80
	v_cvt_f32_ubyte3_e32 v79, v80
	v_cvt_f32_ubyte2_e32 v78, v80
	v_pk_fma_f32 v[176:177], v[174:175], v[68:69], v[184:185] op_sel_hi:[1,0,0]
	v_pk_fma_f32 v[172:173], v[172:173], v[68:69], v[184:185] op_sel_hi:[1,0,0]
	v_cvt_f32_ubyte2_e32 v80, v73
	v_pk_fma_f32 v[174:175], v[78:79], v[66:67], v[172:173] op_sel_hi:[1,0,1]
	v_pk_fma_f32 v[172:173], v[70:71], v[66:67], v[176:177] op_sel_hi:[1,0,1]
	v_cvt_f32_ubyte1_e32 v177, v73
	v_cvt_f32_ubyte0_e32 v176, v73
	v_cvt_f32_ubyte1_e32 v71, v81
	v_cvt_f32_ubyte0_e32 v70, v81
	v_cvt_f32_ubyte3_e32 v79, v81
	v_cvt_f32_ubyte2_e32 v78, v81
	v_cvt_f32_ubyte3_e32 v81, v73
	v_pk_fma_f32 v[176:177], v[176:177], v[68:69], v[184:185] op_sel_hi:[1,0,0]
	v_pk_fma_f32 v[72:73], v[80:81], v[68:69], v[184:185] op_sel_hi:[1,0,0]
	v_pk_fma_f32 v[70:71], v[70:71], v[66:67], v[176:177] op_sel_hi:[1,0,1]
	v_cvt_f32_ubyte3_e32 v177, v74
	v_cvt_f32_ubyte2_e32 v176, v74
	v_cvt_f32_ubyte1_e32 v179, v74
	v_cvt_f32_ubyte0_e32 v178, v74
	v_pk_fma_f32 v[72:73], v[78:79], v[66:67], v[72:73] op_sel_hi:[1,0,1]
	v_cvt_f32_ubyte1_e32 v79, v82
	v_cvt_f32_ubyte0_e32 v78, v82
	v_cvt_f32_ubyte3_e32 v81, v82
	v_cvt_f32_ubyte2_e32 v80, v82
	v_pk_fma_f32 v[178:179], v[178:179], v[68:69], v[184:185] op_sel_hi:[1,0,0]
	v_pk_fma_f32 v[176:177], v[176:177], v[68:69], v[184:185] op_sel_hi:[1,0,0]
	v_pk_fma_f32 v[78:79], v[78:79], v[66:67], v[178:179] op_sel_hi:[1,0,1]
	v_pk_fma_f32 v[80:81], v[80:81], v[66:67], v[176:177] op_sel_hi:[1,0,1]
	v_cvt_f32_ubyte1_e32 v177, v83
	v_cvt_f32_ubyte0_e32 v176, v83
	v_cvt_f32_ubyte3_e32 v179, v83
	v_cvt_f32_ubyte2_e32 v178, v83
	v_cvt_f32_ubyte3_e32 v83, v75
	v_cvt_f32_ubyte2_e32 v82, v75
	v_cvt_f32_ubyte1_e32 v181, v75
	v_cvt_f32_ubyte0_e32 v180, v75
	v_pk_fma_f32 v[74:75], v[180:181], v[68:69], v[184:185] op_sel_hi:[1,0,0]
	v_pk_fma_f32 v[82:83], v[82:83], v[68:69], v[184:185] op_sel_hi:[1,0,0]
	v_cvt_f32_ubyte3_e32 v181, v76
	v_cvt_f32_ubyte2_e32 v180, v76
	v_cvt_f32_ubyte1_e32 v183, v76
	v_cvt_f32_ubyte0_e32 v182, v76
	v_pk_fma_f32 v[178:179], v[178:179], v[66:67], v[82:83] op_sel_hi:[1,0,1]
	v_pk_fma_f32 v[176:177], v[176:177], v[66:67], v[74:75] op_sel_hi:[1,0,1]
	v_cvt_f32_ubyte1_e32 v75, v84
	v_cvt_f32_ubyte0_e32 v74, v84
	v_cvt_f32_ubyte3_e32 v83, v84
	v_cvt_f32_ubyte2_e32 v82, v84
	v_pk_fma_f32 v[186:187], v[182:183], v[68:69], v[184:185] op_sel_hi:[1,0,0]
	v_pk_fma_f32 v[180:181], v[180:181], v[68:69], v[184:185] op_sel_hi:[1,0,0]
	v_cvt_f32_ubyte2_e32 v84, v77
	v_pk_fma_f32 v[182:183], v[82:83], v[66:67], v[180:181] op_sel_hi:[1,0,1]
	v_pk_fma_f32 v[180:181], v[74:75], v[66:67], v[186:187] op_sel_hi:[1,0,1]
	v_cvt_f32_ubyte1_e32 v75, v85
	v_cvt_f32_ubyte0_e32 v74, v85
	v_cvt_f32_ubyte3_e32 v83, v85
	v_cvt_f32_ubyte2_e32 v82, v85
	v_cvt_f32_ubyte3_e32 v85, v77
	v_cvt_f32_ubyte1_e32 v187, v77
	v_cvt_f32_ubyte0_e32 v186, v77
	v_pk_fma_f32 v[76:77], v[186:187], v[68:69], v[184:185] op_sel_hi:[1,0,0]
	v_pk_fma_f32 v[68:69], v[84:85], v[68:69], v[184:185] op_sel_hi:[1,0,0]
	s_nop 0
	v_pk_fma_f32 v[68:69], v[82:83], v[66:67], v[68:69] op_sel_hi:[1,0,1]
	v_pk_fma_f32 v[66:67], v[74:75], v[66:67], v[76:77] op_sel_hi:[1,0,1]
	ds_read_b128 v[74:77], v123 offset:128
	ds_read_b128 v[82:85], v123 offset:192
	ds_read_b128 v[184:187], v112 offset:64
	ds_read_b128 v[188:191], v112 offset:4672
	ds_read_b128 v[192:195], v112 offset:9280
	ds_read_b128 v[196:199], v112 offset:13888
	ds_read_b128 v[200:203], v112 offset:18496
	ds_read_b128 v[204:207], v112 offset:23104
	ds_read_b128 v[208:211], v112 offset:27712
	ds_read_b128 v[212:215], v112 offset:32320
	s_waitcnt lgkmcnt(14)
	v_cvt_pk_bf16_f32 v62, v62, v63
	v_cvt_pk_bf16_f32 v63, v64, v65
	v_cvt_pk_bf16_f32 v64, v86, v87
	v_cvt_pk_bf16_f32 v65, v88, v89
	s_nop 1
	v_mfma_f32_16x16x32_bf16 v[86:89], v[90:93], v[62:65], v[164:167]
	v_mfma_f32_16x16x32_bf16 v[90:93], v[136:139], v[62:65], v[168:171]
	v_mfma_f32_16x16x32_bf16 v[136:139], v[140:143], v[62:65], v[172:175]
	v_mfma_f32_16x16x32_bf16 v[70:73], v[144:147], v[62:65], v[70:73]
	s_waitcnt lgkmcnt(13)
	v_mfma_f32_16x16x32_bf16 v[78:81], v[148:151], v[62:65], v[78:81]
	s_waitcnt lgkmcnt(12)
	v_mfma_f32_16x16x32_bf16 v[140:143], v[152:155], v[62:65], v[176:179]
	s_waitcnt lgkmcnt(11)
	v_mfma_f32_16x16x32_bf16 v[144:147], v[156:159], v[62:65], v[180:183]
	s_waitcnt lgkmcnt(10)
	v_mfma_f32_16x16x32_bf16 v[62:65], v[160:163], v[62:65], v[66:69]
	s_nop 2
	ds_read_b128 v[66:69], v123 offset:256
	ds_read_b128 v[148:151], v123 offset:320
	ds_read_b128 v[152:155], v112 offset:128
	ds_read_b128 v[156:159], v112 offset:4736
	ds_read_b128 v[160:163], v112 offset:9344
	ds_read_b128 v[164:167], v112 offset:13952
	ds_read_b128 v[168:171], v112 offset:18560
	ds_read_b128 v[172:175], v112 offset:23168
	ds_read_b128 v[176:179], v112 offset:27776
	ds_read_b128 v[180:183], v112 offset:32384
	s_waitcnt lgkmcnt(14)
	v_cvt_pk_bf16_f32 v74, v74, v75
	v_cvt_pk_bf16_f32 v75, v76, v77
	v_cvt_pk_bf16_f32 v76, v82, v83
	v_cvt_pk_bf16_f32 v77, v84, v85
	s_waitcnt lgkmcnt(10)
	s_nop 0
	v_mfma_f32_16x16x32_bf16 v[62:65], v[212:215], v[74:77], v[62:65]
	v_mfma_f32_16x16x32_bf16 v[82:85], v[184:187], v[74:77], v[86:89]
	v_mfma_f32_16x16x32_bf16 v[86:89], v[188:191], v[74:77], v[90:93]
	v_mfma_f32_16x16x32_bf16 v[90:93], v[192:195], v[74:77], v[136:139]
	v_mfma_f32_16x16x32_bf16 v[70:73], v[196:199], v[74:77], v[70:73]
	v_mfma_f32_16x16x32_bf16 v[78:81], v[200:203], v[74:77], v[78:81]
	v_mfma_f32_16x16x32_bf16 v[136:139], v[204:207], v[74:77], v[140:143]
	v_mfma_f32_16x16x32_bf16 v[140:143], v[208:211], v[74:77], v[144:147]
	ds_read_b128 v[74:77], v123 offset:384
	s_nop 1
	ds_read_b128 v[144:147], v123 offset:448
	ds_read_b128 v[184:187], v112 offset:192
	ds_read_b128 v[188:191], v112 offset:4800
	ds_read_b128 v[192:195], v112 offset:9408
	ds_read_b128 v[196:199], v112 offset:14016
	ds_read_b128 v[200:203], v112 offset:18624
	ds_read_b128 v[204:207], v112 offset:23232
	ds_read_b128 v[208:211], v112 offset:27840
	ds_read_b128 v[212:215], v112 offset:32448
	s_waitcnt lgkmcnt(14)
	v_cvt_pk_bf16_f32 v66, v66, v67
	v_cvt_pk_bf16_f32 v67, v68, v69
	v_cvt_pk_bf16_f32 v68, v148, v149
	v_cvt_pk_bf16_f32 v69, v150, v151
	s_waitcnt lgkmcnt(10)
	s_nop 0
	v_mfma_f32_16x16x32_bf16 v[62:65], v[180:183], v[66:69], v[62:65]
	v_mfma_f32_16x16x32_bf16 v[82:85], v[152:155], v[66:69], v[82:85]
	v_mfma_f32_16x16x32_bf16 v[86:89], v[156:159], v[66:69], v[86:89]
	v_mfma_f32_16x16x32_bf16 v[90:93], v[160:163], v[66:69], v[90:93]
	v_mfma_f32_16x16x32_bf16 v[70:73], v[164:167], v[66:69], v[70:73]
	v_mfma_f32_16x16x32_bf16 v[78:81], v[168:171], v[66:69], v[78:81]
	v_mfma_f32_16x16x32_bf16 v[136:139], v[172:175], v[66:69], v[136:139]
	v_mfma_f32_16x16x32_bf16 v[140:143], v[176:179], v[66:69], v[140:143]
	ds_read2st64_b64 v[66:69], v134 offset0:54 offset1:63
	ds_read2st64_b64 v[148:151], v134 offset0:36 offset1:45
	ds_read2st64_b64 v[152:155], v134 offset0:18 offset1:27
	ds_read2st64_b64 v[156:159], v134 offset1:9
	ds_read_b128 v[160:163], v124 offset:8704
	s_waitcnt lgkmcnt(14)
	v_cvt_pk_bf16_f32 v74, v74, v75
	v_cvt_pk_bf16_f32 v75, v76, v77
	s_waitcnt lgkmcnt(13)
	v_cvt_pk_bf16_f32 v76, v144, v145
	v_cvt_pk_bf16_f32 v77, v146, v147
	s_waitcnt lgkmcnt(5)
	s_nop 0
	v_mfma_f32_16x16x32_bf16 v[62:65], v[212:215], v[74:77], v[62:65]
	v_mfma_f32_16x16x32_bf16 v[82:85], v[184:187], v[74:77], v[82:85]
	v_mfma_f32_16x16x32_bf16 v[86:89], v[188:191], v[74:77], v[86:89]
	v_mfma_f32_16x16x32_bf16 v[90:93], v[192:195], v[74:77], v[90:93]
	v_mfma_f32_16x16x32_bf16 v[70:73], v[196:199], v[74:77], v[70:73]
	v_mfma_f32_16x16x32_bf16 v[78:81], v[200:203], v[74:77], v[78:81]
	v_mfma_f32_16x16x32_bf16 v[136:139], v[204:207], v[74:77], v[136:139]
	v_mfma_f32_16x16x32_bf16 v[140:143], v[208:211], v[74:77], v[140:143]
	ds_read_b128 v[144:147], v125
	ds_read_b128 v[164:167], v126
	ds_read_b128 v[168:171], v127
	ds_read_b128 v[172:175], v128
	ds_read_b128 v[176:179], v129
	ds_read_b128 v[180:183], v130
	ds_read_b128 v[184:187], v131
	ds_read_b128 v[188:191], v132
	ds_read_b128 v[192:195], v112 offset:36864
	ds_read_b128 v[196:199], v112 offset:41472
	ds_read_b128 v[200:203], v112 offset:46080
	ds_read_b128 v[204:207], v112 offset:50688
	ds_read_b128 v[208:211], v112 offset:55296
	ds_read_b128 v[212:215], v112 offset:59904
	ds_read_b128 v[216:219], v112 offset:64512
	ds_read_b128 v[220:223], v113 offset:32256
	s_waitcnt lgkmcnt(14)
	v_cvt_pk_bf16_f32 v74, v160, v161
	v_cvt_pk_bf16_f32 v75, v162, v163
	s_nop 1
	v_mfma_f32_16x16x16_bf16 v[160:163], v[156:157], v[74:75], v[82:85]
	v_mfma_f32_16x16x16_bf16 v[86:89], v[158:159], v[74:75], v[86:89]
	v_mfma_f32_16x16x16_bf16 v[90:93], v[152:153], v[74:75], v[90:93]
	v_mfma_f32_16x16x16_bf16 v[70:73], v[154:155], v[74:75], v[70:73]
	v_mfma_f32_16x16x16_bf16 v[78:81], v[148:149], v[74:75], v[78:81]
	v_mfma_f32_16x16x16_bf16 v[136:139], v[150:151], v[74:75], v[136:139]
	v_mfma_f32_16x16x16_bf16 v[82:85], v[66:67], v[74:75], v[140:143]
	v_mfma_f32_16x16x16_bf16 v[74:77], v[68:69], v[74:75], v[62:65]
	s_nop 2
	v_exp_f32_e32 v62, v160
	v_exp_f32_e32 v63, v161
	v_exp_f32_e32 v64, v162
	v_exp_f32_e32 v65, v163
	v_add_f32_e32 v62, 1.0, v62
	v_add_f32_e32 v63, 1.0, v63
	v_rcp_f32_e32 v62, v62
	v_rcp_f32_e32 v63, v63
	v_add_f32_e32 v64, 1.0, v64
	v_add_f32_e32 v65, 1.0, v65
	v_rcp_f32_e32 v64, v64
	v_rcp_f32_e32 v65, v65
	v_pk_mul_f32 v[62:63], v[160:161], v[62:63]
	v_exp_f32_e32 v66, v86
	v_cvt_pk_bf16_f32 v140, v62, v63
	v_pk_mul_f32 v[62:63], v[162:163], v[64:65]
	v_exp_f32_e32 v64, v88
	v_cvt_pk_bf16_f32 v141, v62, v63
	v_exp_f32_e32 v63, v87
	v_exp_f32_e32 v65, v89
	v_add_f32_e32 v62, 1.0, v66
	v_rcp_f32_e32 v62, v62
	v_add_f32_e32 v63, 1.0, v63
	v_rcp_f32_e32 v63, v63
	v_add_f32_e32 v64, 1.0, v64
	v_add_f32_e32 v65, 1.0, v65
	v_rcp_f32_e32 v64, v64
	v_rcp_f32_e32 v65, v65
	v_pk_mul_f32 v[62:63], v[86:87], v[62:63]
	v_exp_f32_e32 v66, v90
	v_cvt_pk_bf16_f32 v142, v62, v63
	v_pk_mul_f32 v[62:63], v[88:89], v[64:65]
	v_exp_f32_e32 v64, v92
	v_cvt_pk_bf16_f32 v143, v62, v63
	v_exp_f32_e32 v63, v91
	v_exp_f32_e32 v65, v93
	v_add_f32_e32 v62, 1.0, v66
	v_rcp_f32_e32 v62, v62
	v_add_f32_e32 v63, 1.0, v63
	v_rcp_f32_e32 v63, v63
	v_add_f32_e32 v64, 1.0, v64
	v_add_f32_e32 v65, 1.0, v65
	v_rcp_f32_e32 v64, v64
	v_rcp_f32_e32 v65, v65
	v_pk_mul_f32 v[62:63], v[90:91], v[62:63]
	v_exp_f32_e32 v66, v70
	v_cvt_pk_bf16_f32 v86, v62, v63
	v_pk_mul_f32 v[62:63], v[92:93], v[64:65]
	v_exp_f32_e32 v64, v72
	v_cvt_pk_bf16_f32 v87, v62, v63
	v_exp_f32_e32 v63, v71
	v_exp_f32_e32 v65, v73
	v_add_f32_e32 v62, 1.0, v66
	v_rcp_f32_e32 v62, v62
	v_add_f32_e32 v63, 1.0, v63
	v_rcp_f32_e32 v63, v63
	v_add_f32_e32 v64, 1.0, v64
	v_add_f32_e32 v65, 1.0, v65
	v_rcp_f32_e32 v64, v64
	v_rcp_f32_e32 v65, v65
	v_pk_mul_f32 v[62:63], v[70:71], v[62:63]
	v_exp_f32_e32 v66, v78
	v_cvt_pk_bf16_f32 v88, v62, v63
	v_pk_mul_f32 v[62:63], v[72:73], v[64:65]
	v_exp_f32_e32 v64, v80
	v_cvt_pk_bf16_f32 v89, v62, v63
	v_exp_f32_e32 v63, v79
	v_exp_f32_e32 v65, v81
	v_add_f32_e32 v62, 1.0, v66
	v_rcp_f32_e32 v62, v62
	v_add_f32_e32 v63, 1.0, v63
	v_rcp_f32_e32 v63, v63
	v_add_f32_e32 v64, 1.0, v64
	v_add_f32_e32 v65, 1.0, v65
	v_rcp_f32_e32 v64, v64
	v_rcp_f32_e32 v65, v65
	v_exp_f32_e32 v66, v136
	v_pk_mul_f32 v[62:63], v[78:79], v[62:63]
	v_exp_f32_e32 v67, v139
	v_cvt_pk_bf16_f32 v148, v62, v63
	v_pk_mul_f32 v[62:63], v[80:81], v[64:65]
	v_exp_f32_e32 v65, v137
	v_add_f32_e32 v64, 1.0, v66
	v_exp_f32_e32 v66, v138
	v_rcp_f32_e32 v64, v64
	v_add_f32_e32 v65, 1.0, v65
	v_rcp_f32_e32 v65, v65
	v_add_f32_e32 v66, 1.0, v66
	v_add_f32_e32 v67, 1.0, v67
	v_rcp_f32_e32 v66, v66
	v_rcp_f32_e32 v67, v67
	v_cvt_pk_bf16_f32 v149, v62, v63
	v_pk_mul_f32 v[62:63], v[136:137], v[64:65]
	s_nop 0
	v_cvt_pk_bf16_f32 v150, v62, v63
	v_pk_mul_f32 v[62:63], v[138:139], v[66:67]
	s_nop 0
	v_cvt_pk_bf16_f32 v151, v62, v63
	ds_read_b128 v[90:93], v112 offset:36928
	ds_read_b128 v[136:139], v112 offset:41536
	ds_read_b128 v[152:155], v112 offset:46144
	ds_read_b128 v[156:159], v112 offset:50752
	ds_read_b128 v[160:163], v112 offset:55360
	ds_read_b128 v[224:227], v112 offset:59968
	ds_read_b128 v[228:231], v112 offset:64576
	ds_read_b128 v[232:235], v113 offset:32320
	ds_read_b128 v[62:65], v123
	ds_read_b128 v[66:69], v123 offset:64
	s_waitcnt lgkmcnt(14)
	v_mfma_f32_16x16x32_bf16 v[144:147], v[192:195], v[140:143], v[144:147]
	v_mfma_f32_16x16x32_bf16 v[164:167], v[196:199], v[140:143], v[164:167]
	v_mfma_f32_16x16x32_bf16 v[168:171], v[200:203], v[140:143], v[168:171]
	v_mfma_f32_16x16x32_bf16 v[172:175], v[204:207], v[140:143], v[172:175]
	s_waitcnt lgkmcnt(13)
	v_mfma_f32_16x16x32_bf16 v[176:179], v[208:211], v[140:143], v[176:179]
	s_waitcnt lgkmcnt(12)
	v_mfma_f32_16x16x32_bf16 v[180:183], v[212:215], v[140:143], v[180:183]
	s_waitcnt lgkmcnt(11)
	v_mfma_f32_16x16x32_bf16 v[184:187], v[216:219], v[140:143], v[184:187]
	s_waitcnt lgkmcnt(10)
	v_mfma_f32_16x16x32_bf16 v[140:143], v[220:223], v[140:143], v[188:191]
	s_nop 2
	ds_read_b128 v[188:191], v112 offset:36992
	ds_read_b128 v[192:195], v112 offset:41600
	ds_read_b128 v[196:199], v112 offset:46208
	ds_read_b128 v[200:203], v112 offset:50816
	ds_read_b128 v[204:207], v112 offset:55424
	ds_read_b128 v[208:211], v112 offset:60032
	ds_read_b128 v[212:215], v112 offset:64640
	ds_read_b128 v[216:219], v113 offset:32384
	ds_read_b128 v[70:73], v123 offset:128
	ds_read_b128 v[78:81], v123 offset:192
	s_waitcnt lgkmcnt(14)
	v_mfma_f32_16x16x32_bf16 v[144:147], v[90:93], v[86:89], v[144:147]
	v_mfma_f32_16x16x32_bf16 v[136:139], v[136:139], v[86:89], v[164:167]
	v_mfma_f32_16x16x32_bf16 v[152:155], v[152:155], v[86:89], v[168:171]
	v_mfma_f32_16x16x32_bf16 v[156:159], v[156:159], v[86:89], v[172:175]
	v_mfma_f32_16x16x32_bf16 v[160:163], v[160:163], v[86:89], v[176:179]
	v_mfma_f32_16x16x32_bf16 v[164:167], v[224:227], v[86:89], v[180:183]
	s_waitcnt lgkmcnt(13)
	v_mfma_f32_16x16x32_bf16 v[168:171], v[228:231], v[86:89], v[184:187]
	s_waitcnt lgkmcnt(12)
	v_mfma_f32_16x16x32_bf16 v[140:143], v[232:235], v[86:89], v[140:143]
	ds_read_b128 v[172:175], v112 offset:37056
	ds_read_b128 v[176:179], v112 offset:41664
	ds_read_b128 v[180:183], v112 offset:46272
	ds_read_b128 v[184:187], v112 offset:50880
	ds_read_b128 v[220:223], v112 offset:55488
	ds_read_b128 v[224:227], v112 offset:60096
	ds_read_b128 v[228:231], v112 offset:64704
	ds_read_b128 v[232:235], v113 offset:32448
	ds_read_b128 v[86:89], v123 offset:256
	ds_read_b128 v[90:93], v123 offset:320
	s_waitcnt lgkmcnt(14)
	v_mfma_f32_16x16x32_bf16 v[144:147], v[188:191], v[148:151], v[144:147]
	v_mfma_f32_16x16x32_bf16 v[136:139], v[192:195], v[148:151], v[136:139]
	v_mfma_f32_16x16x32_bf16 v[152:155], v[196:199], v[148:151], v[152:155]
	v_mfma_f32_16x16x32_bf16 v[156:159], v[200:203], v[148:151], v[156:159]
	v_mfma_f32_16x16x32_bf16 v[160:163], v[204:207], v[148:151], v[160:163]
	v_mfma_f32_16x16x32_bf16 v[164:167], v[208:211], v[148:151], v[164:167]
	s_waitcnt lgkmcnt(13)
	v_mfma_f32_16x16x32_bf16 v[168:171], v[212:215], v[148:151], v[168:171]
	s_waitcnt lgkmcnt(12)
	v_mfma_f32_16x16x32_bf16 v[140:143], v[216:219], v[148:151], v[140:143]
	v_exp_f32_e32 v148, v82
	v_exp_f32_e32 v149, v83
	v_exp_f32_e32 v150, v84
	v_exp_f32_e32 v151, v85
	v_add_f32_e32 v148, 1.0, v148
	v_add_f32_e32 v149, 1.0, v149
	v_rcp_f32_e32 v148, v148
	v_rcp_f32_e32 v149, v149
	v_add_f32_e32 v150, 1.0, v150
	v_add_f32_e32 v151, 1.0, v151
	v_rcp_f32_e32 v150, v150
	v_rcp_f32_e32 v151, v151
	v_pk_mul_f32 v[82:83], v[82:83], v[148:149]
	v_exp_f32_e32 v148, v74
	v_cvt_pk_bf16_f32 v82, v82, v83
	v_pk_mul_f32 v[84:85], v[84:85], v[150:151]
	v_exp_f32_e32 v149, v77
	v_cvt_pk_bf16_f32 v83, v84, v85
	v_exp_f32_e32 v85, v75
	v_add_f32_e32 v84, 1.0, v148
	v_exp_f32_e32 v148, v76
	v_rcp_f32_e32 v84, v84
	v_add_f32_e32 v85, 1.0, v85
	v_rcp_f32_e32 v85, v85
	v_add_f32_e32 v148, 1.0, v148
	v_rcp_f32_e32 v192, v148
	v_add_f32_e32 v148, 1.0, v149
	v_rcp_f32_e32 v193, v148
	ds_read_b128 v[148:151], v123 offset:384
	ds_read_b128 v[188:191], v123 offset:448
	v_pk_mul_f32 v[74:75], v[74:75], v[84:85]
	s_nop 0
	v_cvt_pk_bf16_f32 v84, v74, v75
	v_pk_mul_f32 v[74:75], v[76:77], v[192:193]
	s_nop 0
	v_cvt_pk_bf16_f32 v85, v74, v75
	s_waitcnt lgkmcnt(11)
	s_nop 0
	v_mfma_f32_16x16x32_bf16 v[74:77], v[172:175], v[82:85], v[144:147]
	s_waitcnt lgkmcnt(10)
	v_mfma_f32_16x16x32_bf16 v[136:139], v[176:179], v[82:85], v[136:139]
	s_waitcnt lgkmcnt(9)
	v_mfma_f32_16x16x32_bf16 v[144:147], v[180:183], v[82:85], v[152:155]
	s_waitcnt lgkmcnt(8)
	v_mfma_f32_16x16x32_bf16 v[152:155], v[184:187], v[82:85], v[156:159]
	s_waitcnt lgkmcnt(7)
	v_mfma_f32_16x16x32_bf16 v[156:159], v[220:223], v[82:85], v[160:163]
	s_waitcnt lgkmcnt(6)
	v_mfma_f32_16x16x32_bf16 v[160:163], v[224:227], v[82:85], v[164:167]
	s_waitcnt lgkmcnt(5)
	v_mfma_f32_16x16x32_bf16 v[164:167], v[228:231], v[82:85], v[168:171]
	s_waitcnt lgkmcnt(4)
	v_mfma_f32_16x16x32_bf16 v[82:85], v[232:235], v[82:85], v[140:143]
	s_nop 2
	v_exp_f32_e32 v140, v74
	v_exp_f32_e32 v141, v75
	v_exp_f32_e32 v168, v136
	v_exp_f32_e32 v169, v137
	v_exp_f32_e32 v170, v138
	v_exp_f32_e32 v171, v139
	v_exp_f32_e32 v142, v76
	v_exp_f32_e32 v143, v77
	v_add_f32_e32 v140, 1.0, v140
	v_add_f32_e32 v141, 1.0, v141
	v_rcp_f32_e32 v140, v140
	v_rcp_f32_e32 v141, v141
	v_add_f32_e32 v168, 1.0, v168
	v_add_f32_e32 v169, 1.0, v169
	v_rcp_f32_e32 v168, v168
	v_rcp_f32_e32 v169, v169
	v_pk_add_f32 v[170:171], v[170:171], 1.0 op_sel_hi:[1,0]
	v_pk_add_f32 v[142:143], v[142:143], 1.0 op_sel_hi:[1,0]
	v_rcp_f32_e32 v170, v170
	v_rcp_f32_e32 v171, v171
	v_rcp_f32_e32 v142, v142
	v_rcp_f32_e32 v143, v143
	v_exp_f32_e32 v172, v144
	v_exp_f32_e32 v173, v145
	v_pk_mul_f32 v[74:75], v[74:75], v[140:141]
	v_pk_mul_f32 v[136:137], v[136:137], v[168:169]
	v_pk_fma_f32 v[62:63], v[74:75], s[2:3], v[62:63] op_sel_hi:[1,0,1]
	v_exp_f32_e32 v174, v146
	v_pk_mul_f32 v[236:237], v[62:63], v[62:63]
	v_pk_add_f32 v[238:239], v[62:63], 0 op_sel_hi:[1,0]
	v_exp_f32_e32 v175, v147
	v_pk_fma_f32 v[66:67], v[136:137], s[2:3], v[66:67] op_sel_hi:[1,0,1]
	v_pk_mul_f32 v[136:137], v[138:139], v[170:171]
	v_pk_fma_f32 v[236:237], v[66:67], v[66:67], v[236:237]
	v_pk_add_f32 v[238:239], v[66:67], v[238:239]
	v_pk_fma_f32 v[68:69], v[136:137], s[2:3], v[68:69] op_sel_hi:[1,0,1]
	v_pk_mul_f32 v[74:75], v[76:77], v[142:143]
	v_pk_fma_f32 v[236:237], v[68:69], v[68:69], v[236:237]
	v_pk_add_f32 v[238:239], v[68:69], v[238:239]
	v_pk_add_f32 v[172:173], v[172:173], 1.0 op_sel_hi:[1,0]
	v_exp_f32_e32 v176, v152
	v_exp_f32_e32 v177, v153
	v_pk_fma_f32 v[64:65], v[74:75], s[2:3], v[64:65] op_sel_hi:[1,0,1]
	v_rcp_f32_e32 v172, v172
	v_pk_fma_f32 v[236:237], v[64:65], v[64:65], v[236:237]
	v_pk_add_f32 v[238:239], v[64:65], v[238:239]
	v_rcp_f32_e32 v173, v173
	v_pk_add_f32 v[174:175], v[174:175], 1.0 op_sel_hi:[1,0]
	v_exp_f32_e32 v178, v154
	v_exp_f32_e32 v179, v155
	v_rcp_f32_e32 v174, v174
	v_rcp_f32_e32 v175, v175
	v_pk_add_f32 v[176:177], v[176:177], 1.0 op_sel_hi:[1,0]
	v_exp_f32_e32 v180, v156
	v_exp_f32_e32 v181, v157
	v_rcp_f32_e32 v176, v176
	v_rcp_f32_e32 v177, v177
	v_pk_mul_f32 v[144:145], v[144:145], v[172:173]
	v_pk_add_f32 v[178:179], v[178:179], 1.0 op_sel_hi:[1,0]
	v_exp_f32_e32 v182, v158
	v_exp_f32_e32 v183, v159
	v_pk_fma_f32 v[70:71], v[144:145], s[2:3], v[70:71] op_sel_hi:[1,0,1]
	v_rcp_f32_e32 v178, v178
	v_pk_fma_f32 v[236:237], v[70:71], v[70:71], v[236:237]
	v_pk_add_f32 v[238:239], v[70:71], v[238:239]
	v_rcp_f32_e32 v179, v179
	v_pk_mul_f32 v[144:145], v[146:147], v[174:175]
	v_pk_add_f32 v[180:181], v[180:181], 1.0 op_sel_hi:[1,0]
	v_exp_f32_e32 v184, v160
	v_exp_f32_e32 v185, v161
	v_pk_fma_f32 v[72:73], v[144:145], s[2:3], v[72:73] op_sel_hi:[1,0,1]
	v_rcp_f32_e32 v180, v180
	v_pk_fma_f32 v[236:237], v[72:73], v[72:73], v[236:237]
	v_pk_add_f32 v[238:239], v[72:73], v[238:239]
	v_rcp_f32_e32 v181, v181
	v_pk_mul_f32 v[152:153], v[152:153], v[176:177]
	v_pk_add_f32 v[182:183], v[182:183], 1.0 op_sel_hi:[1,0]
	v_exp_f32_e32 v186, v162
	v_exp_f32_e32 v187, v163
	v_pk_fma_f32 v[78:79], v[152:153], s[2:3], v[78:79] op_sel_hi:[1,0,1]
	v_rcp_f32_e32 v182, v182
	v_pk_fma_f32 v[236:237], v[78:79], v[78:79], v[236:237]
	v_pk_add_f32 v[238:239], v[78:79], v[238:239]
	v_rcp_f32_e32 v183, v183
	v_pk_mul_f32 v[152:153], v[154:155], v[178:179]
	v_pk_add_f32 v[184:185], v[184:185], 1.0 op_sel_hi:[1,0]
	v_exp_f32_e32 v192, v164
	v_exp_f32_e32 v193, v165
	v_pk_fma_f32 v[80:81], v[152:153], s[2:3], v[80:81] op_sel_hi:[1,0,1]
	v_rcp_f32_e32 v184, v184
	v_pk_fma_f32 v[236:237], v[80:81], v[80:81], v[236:237]
	v_pk_add_f32 v[238:239], v[80:81], v[238:239]
	v_rcp_f32_e32 v185, v185
	v_pk_mul_f32 v[156:157], v[156:157], v[180:181]
	v_pk_add_f32 v[186:187], v[186:187], 1.0 op_sel_hi:[1,0]
	v_exp_f32_e32 v194, v166
	v_exp_f32_e32 v195, v167
	s_waitcnt lgkmcnt(3)
	v_pk_fma_f32 v[86:87], v[156:157], s[2:3], v[86:87] op_sel_hi:[1,0,1]
	v_rcp_f32_e32 v186, v186
	v_pk_fma_f32 v[236:237], v[86:87], v[86:87], v[236:237]
	v_pk_add_f32 v[238:239], v[86:87], v[238:239]
	v_rcp_f32_e32 v187, v187
	v_pk_mul_f32 v[156:157], v[158:159], v[182:183]
	v_pk_add_f32 v[192:193], v[192:193], 1.0 op_sel_hi:[1,0]
	v_exp_f32_e32 v196, v82
	v_exp_f32_e32 v197, v83
	v_pk_fma_f32 v[88:89], v[156:157], s[2:3], v[88:89] op_sel_hi:[1,0,1]
	v_rcp_f32_e32 v192, v192
	v_pk_fma_f32 v[236:237], v[88:89], v[88:89], v[236:237]
	v_pk_add_f32 v[238:239], v[88:89], v[238:239]
	v_rcp_f32_e32 v193, v193
	v_pk_mul_f32 v[160:161], v[160:161], v[184:185]
	v_pk_add_f32 v[194:195], v[194:195], 1.0 op_sel_hi:[1,0]
	v_exp_f32_e32 v198, v84
	v_exp_f32_e32 v199, v85
	s_waitcnt lgkmcnt(2)
	v_pk_fma_f32 v[90:91], v[160:161], s[2:3], v[90:91] op_sel_hi:[1,0,1]
	v_rcp_f32_e32 v194, v194
	v_pk_fma_f32 v[236:237], v[90:91], v[90:91], v[236:237]
	v_pk_add_f32 v[238:239], v[90:91], v[238:239]
	v_rcp_f32_e32 v195, v195
	v_pk_mul_f32 v[160:161], v[162:163], v[186:187]
	v_pk_add_f32 v[196:197], v[196:197], 1.0 op_sel_hi:[1,0]
	v_pk_fma_f32 v[92:93], v[160:161], s[2:3], v[92:93] op_sel_hi:[1,0,1]
	v_rcp_f32_e32 v196, v196
	v_pk_fma_f32 v[236:237], v[92:93], v[92:93], v[236:237]
	v_pk_add_f32 v[238:239], v[92:93], v[238:239]
	v_rcp_f32_e32 v197, v197
	v_pk_mul_f32 v[164:165], v[164:165], v[192:193]
	v_pk_add_f32 v[198:199], v[198:199], 1.0 op_sel_hi:[1,0]
	s_waitcnt lgkmcnt(1)
	v_pk_fma_f32 v[148:149], v[164:165], s[2:3], v[148:149] op_sel_hi:[1,0,1]
	v_rcp_f32_e32 v198, v198
	v_pk_fma_f32 v[236:237], v[148:149], v[148:149], v[236:237]
	v_pk_add_f32 v[238:239], v[148:149], v[238:239]
	v_rcp_f32_e32 v199, v199
	v_pk_mul_f32 v[164:165], v[166:167], v[194:195]
	s_nop 0
	v_pk_fma_f32 v[150:151], v[164:165], s[2:3], v[150:151] op_sel_hi:[1,0,1]
	v_pk_mul_f32 v[82:83], v[82:83], v[196:197]
	v_pk_fma_f32 v[236:237], v[150:151], v[150:151], v[236:237]
	v_pk_add_f32 v[238:239], v[150:151], v[238:239]
	s_waitcnt lgkmcnt(0)
	v_pk_fma_f32 v[82:83], v[82:83], s[2:3], v[188:189] op_sel_hi:[1,0,1]
	v_pk_mul_f32 v[84:85], v[84:85], v[198:199]
	v_pk_fma_f32 v[236:237], v[82:83], v[82:83], v[236:237]
	v_pk_fma_f32 v[84:85], v[84:85], s[2:3], v[190:191] op_sel_hi:[1,0,1]
	v_pk_add_f32 v[238:239], v[82:83], v[238:239]
	v_pk_fma_f32 v[236:237], v[84:85], v[84:85], v[236:237]
	v_pk_add_f32 v[238:239], v[84:85], v[238:239]
	v_add_f32_e32 v75, v236, v237
	v_add_f32_e32 v74, v238, v239
	s_nop 1
	v_permlane16_swap_b32_e32 v74, v75
	s_nop 0
	v_add_f32_e32 v74, v74, v75
	v_mov_b32_e32 v75, v74
	s_nop 1
	v_permlane32_swap_b32_e32 v74, v75
	s_nop 0
	v_add_f32_e32 v74, v74, v75
	v_mov_b32_e32 v75, v74
	s_nop 1
	v_permlane16_swap_b32_e32 v74, v75
	s_nop 0
	v_mul_f32_e32 v74, 0x3c000000, v74
	v_mul_f32_e32 v75, 0x3c000000, v75
	v_fma_f32 v75, -v74, v74, v75
	v_add_f32_e32 v75, 0x3727c5ac, v75
	v_rsq_f32_e32 v76, v75
	s_nop 0
	v_mul_f32_e64 v236, -v74, v76
	v_pk_fma_f32 v[62:63], v[62:63], v[76:77], v[236:237] op_sel_hi:[1,0,0]
	v_pk_fma_f32 v[64:65], v[64:65], v[76:77], v[236:237] op_sel_hi:[1,0,0]
	v_pk_fma_f32 v[66:67], v[66:67], v[76:77], v[236:237] op_sel_hi:[1,0,0]
	v_pk_fma_f32 v[68:69], v[68:69], v[76:77], v[236:237] op_sel_hi:[1,0,0]
	ds_write_b128 v123, v[62:65]
	v_pk_fma_f32 v[70:71], v[70:71], v[76:77], v[236:237] op_sel_hi:[1,0,0]
	v_pk_fma_f32 v[72:73], v[72:73], v[76:77], v[236:237] op_sel_hi:[1,0,0]
	ds_write_b128 v123, v[66:69] offset:64
	v_pk_fma_f32 v[78:79], v[78:79], v[76:77], v[236:237] op_sel_hi:[1,0,0]
	v_pk_fma_f32 v[80:81], v[80:81], v[76:77], v[236:237] op_sel_hi:[1,0,0]
	ds_write_b128 v123, v[70:73] offset:128
	v_pk_fma_f32 v[86:87], v[86:87], v[76:77], v[236:237] op_sel_hi:[1,0,0]
	v_pk_fma_f32 v[88:89], v[88:89], v[76:77], v[236:237] op_sel_hi:[1,0,0]
	ds_write_b128 v123, v[78:81] offset:192
	v_pk_fma_f32 v[90:91], v[90:91], v[76:77], v[236:237] op_sel_hi:[1,0,0]
	v_pk_fma_f32 v[92:93], v[92:93], v[76:77], v[236:237] op_sel_hi:[1,0,0]
	ds_write_b128 v123, v[86:89] offset:256
	v_pk_fma_f32 v[148:149], v[148:149], v[76:77], v[236:237] op_sel_hi:[1,0,0]
	v_pk_fma_f32 v[150:151], v[150:151], v[76:77], v[236:237] op_sel_hi:[1,0,0]
	ds_write_b128 v123, v[90:93] offset:320
	v_pk_fma_f32 v[82:83], v[82:83], v[76:77], v[236:237] op_sel_hi:[1,0,0]
	v_pk_fma_f32 v[84:85], v[84:85], v[76:77], v[236:237] op_sel_hi:[1,0,0]
	ds_write_b128 v123, v[148:151] offset:384
	ds_write_b128 v123, v[82:85] offset:448
	ds_read_b128 v[62:65], v121
	ds_read_b128 v[66:69], v121 offset:1088
	ds_read_b128 v[70:73], v121 offset:2176
	ds_read_b128 v[74:77], v121 offset:3264
	ds_read_b128 v[78:81], v121 offset:4352
	ds_read_b128 v[82:85], v121 offset:5440
	ds_read_b128 v[86:89], v121 offset:6528
	ds_read_b128 v[90:93], v121 offset:7616
	v_add_u32_e32 v136, 0xffffe400, v118
	s_waitcnt lgkmcnt(7)
	v_pk_fma_f32 v[64:65], v[56:57], v[64:65], v[60:61]
	v_pk_fma_f32 v[62:63], v[54:55], v[62:63], v[58:59]
	buffer_store_dwordx4 v[62:65], v136, s[4:7], 0 offen sc0 nt sc1
	v_cmp_lt_i32_e32 vcc, s8, v0
	s_or_b64 s[0:1], vcc, s[0:1]
	s_waitcnt lgkmcnt(6)
	v_pk_fma_f32 v[64:65], v[56:57], v[68:69], v[60:61]
	v_pk_fma_f32 v[62:63], v[54:55], v[66:67], v[58:59]
	v_add_u32_e32 v66, 0xffffe800, v118
	buffer_store_dwordx4 v[62:65], v66, s[4:7], 0 offen sc0 nt sc1
	v_add_u32_e32 v66, 0xffffec00, v118
	s_waitcnt lgkmcnt(5)
	v_pk_fma_f32 v[64:65], v[56:57], v[72:73], v[60:61]
	v_pk_fma_f32 v[62:63], v[54:55], v[70:71], v[58:59]
	buffer_store_dwordx4 v[62:65], v66, s[4:7], 0 offen sc0 nt sc1
	v_add_u32_e32 v66, 0xfffff000, v118
	s_waitcnt lgkmcnt(4)
	v_pk_fma_f32 v[64:65], v[56:57], v[76:77], v[60:61]
	v_pk_fma_f32 v[62:63], v[54:55], v[74:75], v[58:59]
	buffer_store_dwordx4 v[62:65], v66, s[4:7], 0 offen sc0 nt sc1
	v_add_u32_e32 v66, 0xfffff400, v118
	s_waitcnt lgkmcnt(3)
	v_pk_fma_f32 v[64:65], v[56:57], v[80:81], v[60:61]
	v_pk_fma_f32 v[62:63], v[54:55], v[78:79], v[58:59]
	buffer_store_dwordx4 v[62:65], v66, s[4:7], 0 offen sc0 nt sc1
	v_add_u32_e32 v66, 0xfffff800, v118
	s_waitcnt lgkmcnt(2)
	v_pk_fma_f32 v[64:65], v[56:57], v[84:85], v[60:61]
	v_pk_fma_f32 v[62:63], v[54:55], v[82:83], v[58:59]
	buffer_store_dwordx4 v[62:65], v66, s[4:7], 0 offen sc0 nt sc1
	v_add_u32_e32 v66, 0xfffffc00, v118
	s_waitcnt lgkmcnt(1)
	v_pk_fma_f32 v[64:65], v[56:57], v[88:89], v[60:61]
	v_pk_fma_f32 v[62:63], v[54:55], v[86:87], v[58:59]
	buffer_store_dwordx4 v[62:65], v66, s[4:7], 0 offen sc0 nt sc1
	s_waitcnt lgkmcnt(0)
	s_nop 0
	v_pk_fma_f32 v[64:65], v[56:57], v[92:93], v[60:61]
	v_pk_fma_f32 v[62:63], v[54:55], v[90:91], v[58:59]
	buffer_store_dwordx4 v[62:65], v118, s[4:7], 0 offen sc0 nt sc1
	v_add_u32_e32 v118, 0x1000000, v118
	s_nop 0
	v_mov_b32_e32 v62, v0
	s_waitcnt vmcnt(21)
	v_mov_b32_e32 v64, v135
	s_andn2_b64 exec, exec, s[0:1]
	s_cbranch_execnz .LBB1_6
